# HGRN output pass: loop-top waits sized for the steady state (no longer wait for the previous sub-chunk's 32 output stores), first sub-chunk's loads drained before the loop
# baseline (speedup 1.0000x reference)
.LBB0_996:
	s_andn2_b64 vcc, exec, s[0:1]
	s_cbranch_vccnz .LBB0_913
	s_lshl_b32 s0, s2, 2
	s_add_i32 s0, s42, s0
	s_ashr_i32 s1, s0, 31
	s_lshr_b32 s3, s1, 26
	s_add_i32 s22, s0, s3
	s_and_b32 s3, s22, 0x1ffffc0
	s_sub_i32 s3, s0, s3
	s_lshl_b32 s23, s22, 5
	s_and_b32 s23, s23, 0xffffe000
	s_lshl_b32 s3, s3, 7
	s_and_b32 s22, s22, 0xc0
	s_add_i32 s3, s23, s3
	s_add_i32 s23, s22, s85
	s_waitcnt vmcnt(1)
	v_add_u32_e32 v2, s23, v67
	v_readlane_b32 s14, v253, 5
	s_mulk_i32 s42, 0x7c00
	v_ashrrev_i32_e32 v3, 31, v2
	v_readlane_b32 s15, v253, 6
	s_add_i32 s23, s42, 0
	v_and_b32_e32 v66, 31, v67
	v_ashrrev_i32_e32 v70, 5, v67
	v_lshl_add_u64 v[2:3], v[2:3], 2, s[14:15]
	s_add_i32 s24, s23, 0x4400
	s_lshl_b64 s[0:1], s[0:1], 14
	v_readlane_b32 s14, v253, 25
	v_lshl_or_b32 v68, v70, 8, v66
	s_add_u32 s0, s14, s0
	v_readlane_b32 s14, v253, 26
	v_add_u32_e32 v4, 0x400, v68
	s_addc_u32 s1, s14, s1
	v_ashrrev_i32_e32 v5, 31, v4
	v_lshl_add_u64 v[10:11], v[4:5], 2, s[0:1]
	v_add_u32_e32 v4, 0x440, v68
	v_ashrrev_i32_e32 v5, 31, v4
	v_lshl_add_u64 v[12:13], v[4:5], 2, s[0:1]
	v_add_u32_e32 v4, 0x480, v68
	v_ashrrev_i32_e32 v5, 31, v4
	s_waitcnt vmcnt(0)
	v_lshl_add_u64 v[14:15], v[4:5], 2, s[0:1]
	v_add_u32_e32 v4, 0x4c0, v68
	v_ashrrev_i32_e32 v5, 31, v4
	v_lshl_add_u64 v[16:17], v[4:5], 2, s[0:1]
	v_add_u32_e32 v4, 0x600, v68
	v_ashrrev_i32_e32 v5, 31, v4
	v_lshl_add_u64 v[28:29], v[4:5], 2, s[0:1]
	v_add_u32_e32 v4, 0x640, v68
	v_ashrrev_i32_e32 v5, 31, v4
	v_lshl_add_u64 v[30:31], v[4:5], 2, s[0:1]
	v_add_u32_e32 v4, 0x680, v68
	v_ashrrev_i32_e32 v5, 31, v4
	v_ashrrev_i32_e32 v69, 31, v68
	v_lshl_add_u64 v[32:33], v[4:5], 2, s[0:1]
	v_add_u32_e32 v4, 0x6c0, v68
	v_lshl_add_u64 v[26:27], v[68:69], 2, s[0:1]
	v_ashrrev_i32_e32 v5, 31, v4
	v_lshl_add_u64 v[34:35], v[4:5], 2, s[0:1]
	global_load_dword v1, v[2:3], off
	s_nop 0
	global_load_dword v2, v[26:27], off
	global_load_dword v3, v[26:27], off offset:256
	global_load_dword v4, v[26:27], off offset:512
	global_load_dword v5, v[26:27], off offset:768
	global_load_dword v20, v[26:27], off offset:640
	global_load_dword v19, v[26:27], off offset:384
	global_load_dword v18, v[26:27], off offset:128
	global_load_dword v6, v[26:27], off offset:2048
	global_load_dword v7, v[26:27], off offset:2304
	global_load_dword v8, v[26:27], off offset:2560
	global_load_dword v9, v[26:27], off offset:2816
	global_load_dword v24, v[26:27], off offset:2688
	global_load_dword v23, v[26:27], off offset:2432
	global_load_dword v22, v[26:27], off offset:2176
	global_load_dword v21, v[26:27], off offset:896
	s_nop 0
	global_load_dword v10, v[10:11], off
	s_nop 0
	global_load_dword v11, v[12:13], off
	s_nop 0
	global_load_dword v12, v[14:15], off
	global_load_dword v13, v[16:17], off
	s_nop 0
	global_load_dword v14, v[28:29], off
	global_load_dword v15, v[30:31], off
	global_load_dword v16, v[32:33], off
	global_load_dword v25, v[26:27], off offset:2944
	v_add_u32_e32 v26, 0x420, v68
	v_add_u32_e32 v28, 0x460, v68
	v_add_u32_e32 v30, 0x4a0, v68
	v_add_u32_e32 v32, 0x4e0, v68
	v_add_u32_e32 v36, 0x620, v68
	v_add_u32_e32 v38, 0x660, v68
	v_add_u32_e32 v40, 0x6a0, v68
	v_ashrrev_i32_e32 v27, 31, v26
	v_ashrrev_i32_e32 v29, 31, v28
	v_ashrrev_i32_e32 v31, 31, v30
	v_ashrrev_i32_e32 v33, 31, v32
	v_ashrrev_i32_e32 v37, 31, v36
	v_ashrrev_i32_e32 v39, 31, v38
	v_ashrrev_i32_e32 v41, 31, v40
	v_lshl_add_u64 v[26:27], v[26:27], 2, s[0:1]
	v_lshl_add_u64 v[28:29], v[28:29], 2, s[0:1]
	v_lshl_add_u64 v[30:31], v[30:31], 2, s[0:1]
	v_lshl_add_u64 v[32:33], v[32:33], 2, s[0:1]
	v_lshl_add_u64 v[36:37], v[36:37], 2, s[0:1]
	v_lshl_add_u64 v[38:39], v[38:39], 2, s[0:1]
	v_lshl_add_u64 v[40:41], v[40:41], 2, s[0:1]
	global_load_dword v17, v[34:35], off
	s_nop 0
	global_load_dword v26, v[26:27], off
	s_nop 0
	global_load_dword v27, v[28:29], off
	s_nop 0
	global_load_dword v28, v[30:31], off
	global_load_dword v29, v[32:33], off
	s_nop 0
	global_load_dword v30, v[36:37], off
	global_load_dword v31, v[38:39], off
	global_load_dword v32, v[40:41], off
	v_add_u32_e32 v34, 0x6e0, v68
	v_add_u32_e32 v36, 0x800, v68
	v_add_u32_e32 v38, 0x840, v68
	v_add_u32_e32 v40, 0x880, v68
	v_add_u32_e32 v42, 0x8c0, v68
	v_add_u32_e32 v44, 0xa00, v68
	v_add_u32_e32 v46, 0xa40, v68
	v_add_u32_e32 v48, 0xa80, v68
	v_ashrrev_i32_e32 v35, 31, v34
	v_ashrrev_i32_e32 v37, 31, v36
	v_ashrrev_i32_e32 v39, 31, v38
	v_ashrrev_i32_e32 v41, 31, v40
	v_ashrrev_i32_e32 v43, 31, v42
	v_ashrrev_i32_e32 v45, 31, v44
	v_ashrrev_i32_e32 v47, 31, v46
	v_ashrrev_i32_e32 v49, 31, v48
	v_lshl_add_u64 v[34:35], v[34:35], 2, s[0:1]
	v_lshl_add_u64 v[36:37], v[36:37], 2, s[0:1]
	v_lshl_add_u64 v[38:39], v[38:39], 2, s[0:1]
	v_lshl_add_u64 v[40:41], v[40:41], 2, s[0:1]
	v_lshl_add_u64 v[42:43], v[42:43], 2, s[0:1]
	v_lshl_add_u64 v[44:45], v[44:45], 2, s[0:1]
	v_lshl_add_u64 v[46:47], v[46:47], 2, s[0:1]
	v_lshl_add_u64 v[48:49], v[48:49], 2, s[0:1]
	global_load_dword v33, v[34:35], off
	s_nop 0
	global_load_dword v34, v[36:37], off
	global_load_dword v35, v[38:39], off
	s_nop 0
	global_load_dword v36, v[40:41], off
	global_load_dword v37, v[42:43], off
	global_load_dword v38, v[44:45], off
	global_load_dword v39, v[46:47], off
	s_nop 0
	global_load_dword v40, v[48:49], off
	v_add_u32_e32 v42, 0xac0, v68
	v_add_u32_e32 v44, 0xc00, v68
	v_add_u32_e32 v46, 0xc40, v68
	v_add_u32_e32 v48, 0xc80, v68
	v_add_u32_e32 v50, 0xcc0, v68
	v_add_u32_e32 v52, 0xe00, v68
	v_add_u32_e32 v54, 0xe40, v68
	v_add_u32_e32 v56, 0xe80, v68
	v_ashrrev_i32_e32 v43, 31, v42
	v_ashrrev_i32_e32 v45, 31, v44
	v_ashrrev_i32_e32 v47, 31, v46
	v_ashrrev_i32_e32 v49, 31, v48
	v_ashrrev_i32_e32 v51, 31, v50
	v_ashrrev_i32_e32 v53, 31, v52
	v_ashrrev_i32_e32 v55, 31, v54
	v_ashrrev_i32_e32 v57, 31, v56
	v_lshl_add_u64 v[42:43], v[42:43], 2, s[0:1]
	v_lshl_add_u64 v[44:45], v[44:45], 2, s[0:1]
	v_lshl_add_u64 v[46:47], v[46:47], 2, s[0:1]
	v_lshl_add_u64 v[48:49], v[48:49], 2, s[0:1]
	v_lshl_add_u64 v[50:51], v[50:51], 2, s[0:1]
	v_lshl_add_u64 v[52:53], v[52:53], 2, s[0:1]
	v_lshl_add_u64 v[54:55], v[54:55], 2, s[0:1]
	v_lshl_add_u64 v[56:57], v[56:57], 2, s[0:1]
	global_load_dword v41, v[42:43], off
	s_nop 0
	global_load_dword v42, v[44:45], off
	global_load_dword v43, v[46:47], off
	s_nop 0
	global_load_dword v44, v[48:49], off
	global_load_dword v45, v[50:51], off
	global_load_dword v46, v[52:53], off
	global_load_dword v47, v[54:55], off
	s_nop 0
	global_load_dword v48, v[56:57], off
	v_add_u32_e32 v50, 0xec0, v68
	v_add_u32_e32 v52, 0x820, v68
	v_add_u32_e32 v54, 0x860, v68
	v_add_u32_e32 v56, 0x8a0, v68
	v_add_u32_e32 v58, 0x8e0, v68
	v_add_u32_e32 v60, 0xa20, v68
	v_add_u32_e32 v62, 0xa60, v68
	v_add_u32_e32 v64, 0xaa0, v68
	v_ashrrev_i32_e32 v51, 31, v50
	v_ashrrev_i32_e32 v53, 31, v52
	v_ashrrev_i32_e32 v55, 31, v54
	v_ashrrev_i32_e32 v57, 31, v56
	v_ashrrev_i32_e32 v59, 31, v58
	v_ashrrev_i32_e32 v61, 31, v60
	v_ashrrev_i32_e32 v63, 31, v62
	v_ashrrev_i32_e32 v65, 31, v64
	v_lshl_add_u64 v[50:51], v[50:51], 2, s[0:1]
	v_lshl_add_u64 v[52:53], v[52:53], 2, s[0:1]
	v_lshl_add_u64 v[54:55], v[54:55], 2, s[0:1]
	v_lshl_add_u64 v[56:57], v[56:57], 2, s[0:1]
	v_lshl_add_u64 v[58:59], v[58:59], 2, s[0:1]
	v_lshl_add_u64 v[60:61], v[60:61], 2, s[0:1]
	v_lshl_add_u64 v[62:63], v[62:63], 2, s[0:1]
	v_lshl_add_u64 v[64:65], v[64:65], 2, s[0:1]
	global_load_dword v49, v[50:51], off
	s_nop 0
	global_load_dword v50, v[52:53], off
	global_load_dword v51, v[54:55], off
	s_nop 0
	global_load_dword v52, v[56:57], off
	global_load_dword v53, v[58:59], off
	global_load_dword v54, v[60:61], off
	global_load_dword v55, v[62:63], off
	s_nop 0
	global_load_dword v56, v[64:65], off
	v_add_u32_e32 v58, 0xae0, v68
	v_add_u32_e32 v60, 0xc20, v68
	v_add_u32_e32 v62, 0xc60, v68
	v_add_u32_e32 v64, 0xca0, v68
	v_add_u32_e32 v72, 0xce0, v68
	v_add_u32_e32 v74, 0xe20, v68
	v_add_u32_e32 v76, 0xe60, v68
	v_add_u32_e32 v78, 0xea0, v68
	v_add_u32_e32 v68, 0xee0, v68
	v_ashrrev_i32_e32 v59, 31, v58
	v_ashrrev_i32_e32 v61, 31, v60
	v_ashrrev_i32_e32 v63, 31, v62
	v_ashrrev_i32_e32 v65, 31, v64
	v_ashrrev_i32_e32 v69, 31, v68
	v_readlane_b32 s40, v251, 20
	v_lshl_add_u64 v[58:59], v[58:59], 2, s[0:1]
	v_lshl_add_u64 v[60:61], v[60:61], 2, s[0:1]
	v_lshl_add_u64 v[62:63], v[62:63], 2, s[0:1]
	v_lshl_add_u64 v[64:65], v[64:65], 2, s[0:1]
	v_ashrrev_i32_e32 v73, 31, v72
	v_ashrrev_i32_e32 v75, 31, v74
	v_ashrrev_i32_e32 v77, 31, v76
	v_ashrrev_i32_e32 v79, 31, v78
	v_lshl_add_u64 v[68:69], v[68:69], 2, s[0:1]
	v_or_b32_e32 v114, s18, v66
	v_readlane_b32 s42, v251, 22
	v_readlane_b32 s43, v251, 23
	v_lshl_add_u64 v[72:73], v[72:73], 2, s[0:1]
	v_lshl_add_u64 v[74:75], v[74:75], 2, s[0:1]
	v_lshl_add_u64 v[76:77], v[76:77], 2, s[0:1]
	v_lshl_add_u64 v[78:79], v[78:79], 2, s[0:1]
	global_load_dword v57, v[58:59], off
	s_nop 0
	global_load_dword v58, v[60:61], off
	global_load_dword v59, v[62:63], off
	s_nop 0
	global_load_dword v60, v[64:65], off
	global_load_dword v61, v[72:73], off
	global_load_dword v62, v[74:75], off
	global_load_dword v63, v[76:77], off
	s_nop 0
	global_load_dword v64, v[78:79], off
	global_load_dword v65, v[68:69], off
	v_lshl_add_u64 v[68:69], v[114:115], 2, s[42:43]
	v_ashrrev_i32_e32 v177, 3, v67
	global_load_dword v173, v[68:69], off
	global_load_dword v176, v[68:69], off offset:128
	v_add_u32_e32 v71, s3, v177
	v_mov_b64_e32 v[68:69], s[10:11]
	v_mad_i64_i32 v[68:69], s[0:1], v71, s96, v[68:69]
	v_lshlrev_b32_e32 v71, 3, v67
	s_lshl_b32 s80, s22, 1
	v_and_b32_e32 v71, 56, v71
	v_lshl_add_u64 v[68:69], v[68:69], 0, s[80:81]
	v_lshlrev_b32_e32 v114, 1, v71
	v_lshl_add_u64 v[68:69], v[68:69], 0, v[114:115]
	v_add_co_u32_e32 v72, vcc, s33, v68
	global_load_dwordx4 v[98:101], v[68:69], off offset:1728
	global_load_dwordx4 v[102:105], v[68:69], off offset:1216
	v_addc_co_u32_e32 v73, vcc, 0, v69, vcc
	global_load_dwordx4 v[106:109], v[72:73], off offset:1728
	global_load_dwordx4 v[110:113], v[72:73], off offset:2240
	global_load_dwordx4 v[116:119], v[68:69], off offset:2240
	global_load_dwordx4 v[120:123], v[72:73], off offset:1216
	v_add_co_u32_e32 v72, vcc, s84, v68
	s_add_i32 s1, s23, 0x2200
	s_nop 0
	v_addc_co_u32_e32 v73, vcc, 0, v69, vcc
	v_add_co_u32_e32 v68, vcc, s97, v68
	global_load_dwordx4 v[124:127], v[72:73], off offset:1728
	global_load_dwordx4 v[128:131], v[72:73], off offset:1216
	v_addc_co_u32_e32 v69, vcc, 0, v69, vcc
	global_load_dwordx4 v[132:135], v[68:69], off offset:1728
	global_load_dwordx4 v[136:139], v[68:69], off offset:2240
	global_load_dwordx4 v[140:143], v[72:73], off offset:2240
	global_load_dwordx4 v[144:147], v[68:69], off offset:1216
	v_lshl_add_u32 v68, v71, 2, s23
	v_lshlrev_b32_e32 v69, 3, v70
	v_and_b32_e32 v73, 16, v67
	v_mov_b32_e32 v75, s24
	v_mov_b32_e32 v76, s1
	v_cmp_gt_u32_e64 s[38:39], 16, v66
	s_movk_i32 s14, 0x110
	v_add_u32_e32 v73, v69, v73
	v_cndmask_b32_e64 v75, v75, v76, s[38:39]
	v_mad_u64_u32 v[170:171], s[24:25], v177, s14, v[68:69]
	v_mul_u32_u24_e32 v71, 0x4c, v71
	v_lshlrev_b32_e32 v76, 1, v177
	v_readlane_b32 s46, v251, 26
	v_readlane_b32 s47, v251, 27
	v_add3_u32 v171, v68, v71, v76
	v_or_b32_e32 v71, 2, v73
	v_readlane_b32 s48, v251, 28
	v_readlane_b32 s49, v251, 29
	v_cmp_gt_i32_e64 s[46:47], v71, v66
	v_or_b32_e32 v71, 3, v73
	v_readlane_b32 s50, v251, 30
	v_readlane_b32 s51, v251, 31
	v_cmp_gt_i32_e64 s[48:49], v71, v66
	v_or_b32_e32 v71, 4, v73
	v_readlane_b32 s52, v251, 32
	v_readlane_b32 s53, v251, 33
	v_cmp_gt_i32_e64 s[50:51], v71, v66
	v_or_b32_e32 v71, 5, v73
	v_readlane_b32 s54, v251, 34
	v_readlane_b32 s55, v251, 35
	v_lshlrev_b32_e32 v72, 4, v70
	v_mul_u32_u24_e32 v74, 0x44, v66
	v_mul_u32_u24_e32 v68, 40, v66
	v_cmp_gt_i32_e64 s[52:53], v71, v66
	v_or_b32_e32 v71, 6, v73
	v_readlane_b32 s41, v251, 21
	v_add_u32_e32 v180, s23, v72
	v_lshlrev_b32_e32 v74, 2, v74
	v_lshlrev_b32_e32 v68, 1, v68
	v_cmp_gt_i32_e64 s[54:55], v71, v66
	v_or_b32_e32 v71, 7, v73
	s_movk_i32 s1, 0x220
	v_lshl_add_u32 v179, v67, 2, s23
	v_add_u32_e32 v181, s23, v74
	v_cmp_gt_u32_e64 s[40:41], 32, v67
	v_add_u32_e32 v184, v180, v68
	v_cmp_gt_i32_e64 s[56:57], v71, v66
	v_and_b32_e32 v67, 0xffffffe0, v67
	v_add_u32_e32 v68, s23, v68
	v_mul_lo_u32 v71, v70, s1
	s_movk_i32 s1, 0xffb4
	v_add3_u32 v185, v75, v74, v67
	v_add_u32_e32 v186, v181, v67
	v_add_u32_e32 v187, s23, v67
	v_sub_u32_e32 v67, 0, v72
	v_add_u32_e32 v188, v68, v69
	v_add_u32_e32 v72, 0x440, v71
	v_mad_i32_i24 v189, v66, s1, v68
	v_or_b32_e32 v68, v71, v66
	v_lshl_add_u32 v190, v68, 2, s23
	v_or_b32_e32 v68, v72, v66
	v_lshlrev_b32_e32 v183, 2, v70
	v_lshl_add_u32 v192, v68, 2, s23
	v_lshlrev_b32_e32 v68, 2, v66
	v_add_u32_e32 v172, s23, v68
	s_movk_i32 s1, 0x440
	v_or_b32_e32 v196, 1, v183
	v_readlane_b32 s44, v251, 24
	v_readlane_b32 s45, v251, 25
	s_add_u32 s26, s10, s80
	v_mul_lo_u32 v70, v70, s1
	s_waitcnt vmcnt(13)
	v_mad_u64_u32 v[174:175], s[24:25], v196, s14, v[172:173]
	s_addc_u32 s27, s11, 0
	v_cmp_gt_i32_e64 s[42:43], v73, v66
	v_cmp_lt_i32_e64 s[44:45], v73, v66
	v_add_u32_e32 v69, 0xa00, v188
	v_lshl_add_u32 v191, v71, 2, v189
	v_lshl_add_u32 v71, v72, 2, v172
	v_add3_u32 v194, s23, v70, v68
	v_add_u32_e32 v195, v172, v70
	v_add_u32_e32 v68, 0x110, v174
	v_add_u32_e32 v70, 0x220, v174
	v_add_u32_e32 v72, 0x770, v174
	v_add_u32_e32 v74, 0x880, v174
	v_add_u32_e32 v75, 0x990, v174
	v_add_u32_e32 v76, 0xaa0, v174
	v_add_u32_e32 v77, 0xff0, v174
	v_add_u32_e32 v78, 0x1100, v174
	v_add_u32_e32 v79, 0x1210, v174
	v_add_u32_e32 v80, 0x1320, v174
	v_add_u32_e32 v81, 0x1870, v174
	v_add_u32_e32 v82, 0x1980, v174
	v_add_u32_e32 v83, 0x1a90, v174
	v_add_u32_e32 v84, 0x1ba0, v174
	v_mul_lo_u32 v73, v73, s14
	s_mov_b32 s0, 0
	v_lshl_add_u64 v[168:169], s[26:27], 0, v[114:115]
	v_sub_f32_e32 v178, 1.0, v1
	v_add_u32_e32 v182, 32, v177
	v_add_u32_e32 v193, 0x80, v190
	v_or_b32_e32 v175, 2, v183
	v_or_b32_e32 v197, 3, v183
	v_add_u32_e32 v198, s23, v73
	v_add_u32_e32 v199, v186, v67
	s_lshl_b32 s80, s22, 1
	v_lshlrev_b32_e32 v114, 1, v66
	v_add_u32_e32 v200, 0x6000, v69
	v_add_u32_e32 v201, 0x80, v71
	v_add_u32_e32 v202, 0x4400, v68
	v_add_u32_e32 v203, 0x4400, v70
	v_add_u32_e32 v204, 0x4400, v72
	v_add_u32_e32 v205, 0x4400, v74
	v_add_u32_e32 v206, 0x4400, v75
	v_add_u32_e32 v207, 0x4400, v76
	v_add_u32_e32 v208, 0x4400, v77
	v_add_u32_e32 v209, 0x4400, v78
	v_add_u32_e32 v210, 0x4400, v79
	v_add_u32_e32 v211, 0x4400, v80
	v_add_u32_e32 v212, 0x4400, v81
	v_add_u32_e32 v213, 0x4400, v82
	v_add_u32_e32 v214, 0x4400, v83
	v_add_u32_e32 v215, 0x4400, v84
	s_waitcnt vmcnt(0)
.LBB0_998:
	s_waitcnt vmcnt(43)
	v_lshlrev_b32_e32 v66, 16, v98
	v_and_b32_e32 v67, 0xffff0000, v98
	v_lshlrev_b32_e32 v68, 16, v99
	v_and_b32_e32 v69, 0xffff0000, v99
	v_lshlrev_b32_e32 v70, 16, v100
	v_and_b32_e32 v71, 0xffff0000, v100
	v_lshlrev_b32_e32 v72, 16, v101
	v_and_b32_e32 v73, 0xffff0000, v101
	ds_write_b128 v170, v[66:69]
	s_waitcnt vmcnt(42)
	v_lshlrev_b32_e32 v66, 16, v102
	v_and_b32_e32 v67, 0xffff0000, v102
	ds_write_b128 v170, v[70:73] offset:16
	v_lshlrev_b32_e32 v70, 16, v103
	v_and_b32_e32 v71, 0xffff0000, v103
	v_mul_f32_e32 v68, 0xbfb8aa3b, v66
	v_mul_f32_e32 v69, 0xbfb8aa3b, v67
	v_mul_f32_e32 v72, 0xbfb8aa3b, v70
	v_mul_f32_e32 v73, 0xbfb8aa3b, v71
	v_lshlrev_b32_e32 v74, 16, v104
	v_and_b32_e32 v75, 0xffff0000, v104
	v_lshlrev_b32_e32 v78, 16, v105
	v_and_b32_e32 v79, 0xffff0000, v105
	v_exp_f32_e32 v68, v68
	v_exp_f32_e32 v69, v69
	v_exp_f32_e32 v72, v72
	v_exp_f32_e32 v73, v73
	v_mul_f32_e32 v76, 0xbfb8aa3b, v74
	v_mul_f32_e32 v77, 0xbfb8aa3b, v75
	v_mul_f32_e32 v80, 0xbfb8aa3b, v78
	v_mul_f32_e32 v81, 0xbfb8aa3b, v79
	v_exp_f32_e32 v76, v76
	v_exp_f32_e32 v77, v77
	v_exp_f32_e32 v80, v80
	v_exp_f32_e32 v81, v81
	v_add_f32_e32 v68, 1.0, v68
	v_add_f32_e32 v69, 1.0, v69
	v_add_f32_e32 v72, 1.0, v72
	v_add_f32_e32 v73, 1.0, v73
	v_rcp_f32_e32 v68, v68
	v_rcp_f32_e32 v69, v69
	v_rcp_f32_e32 v72, v72
	v_rcp_f32_e32 v73, v73
	v_add_f32_e32 v76, 1.0, v76
	v_add_f32_e32 v77, 1.0, v77
	v_add_f32_e32 v80, 1.0, v80
	v_add_f32_e32 v81, 1.0, v81
	v_rcp_f32_e32 v76, v76
	v_rcp_f32_e32 v77, v77
	v_rcp_f32_e32 v80, v80
	v_rcp_f32_e32 v81, v81
	v_pk_mul_f32 v[66:67], v[68:69], v[66:67]
	v_pk_mul_f32 v[68:69], v[72:73], v[70:71]
	ds_write_b128 v170, v[66:69] offset:17408
	v_pk_mul_f32 v[66:67], v[76:77], v[74:75]
	v_pk_mul_f32 v[68:69], v[80:81], v[78:79]
	ds_write_b128 v170, v[66:69] offset:17424
	s_waitcnt vmcnt(39)
	ds_write_b16 v171, v116 offset:26112
	ds_write_b16_d16_hi v171, v116 offset:26192
	ds_write_b16 v171, v117 offset:26272
	ds_write_b16_d16_hi v171, v117 offset:26352
	ds_write_b16 v171, v118 offset:26432
	ds_write_b16_d16_hi v171, v118 offset:26512
	ds_write_b16 v171, v119 offset:26592
	ds_write_b16_d16_hi v171, v119 offset:26672
	v_lshlrev_b32_e32 v66, 16, v106
	v_and_b32_e32 v67, 0xffff0000, v106
	v_lshlrev_b32_e32 v68, 16, v107
	v_and_b32_e32 v69, 0xffff0000, v107
	v_lshlrev_b32_e32 v70, 16, v108
	v_and_b32_e32 v71, 0xffff0000, v108
	v_lshlrev_b32_e32 v72, 16, v109
	v_and_b32_e32 v73, 0xffff0000, v109
	ds_write_b128 v170, v[66:69] offset:2176
	s_waitcnt vmcnt(38)
	v_lshlrev_b32_e32 v66, 16, v120
	v_and_b32_e32 v67, 0xffff0000, v120
	ds_write_b128 v170, v[70:73] offset:2192
	v_lshlrev_b32_e32 v70, 16, v121
	v_and_b32_e32 v71, 0xffff0000, v121
	v_mul_f32_e32 v68, 0xbfb8aa3b, v66
	v_mul_f32_e32 v69, 0xbfb8aa3b, v67
	v_mul_f32_e32 v72, 0xbfb8aa3b, v70
	v_mul_f32_e32 v73, 0xbfb8aa3b, v71
	v_lshlrev_b32_e32 v74, 16, v122
	v_and_b32_e32 v75, 0xffff0000, v122
	v_lshlrev_b32_e32 v78, 16, v123
	v_and_b32_e32 v79, 0xffff0000, v123
	v_exp_f32_e32 v68, v68
	v_exp_f32_e32 v69, v69
	v_exp_f32_e32 v72, v72
	v_exp_f32_e32 v73, v73
	v_mul_f32_e32 v76, 0xbfb8aa3b, v74
	v_mul_f32_e32 v77, 0xbfb8aa3b, v75
	v_mul_f32_e32 v80, 0xbfb8aa3b, v78
	v_mul_f32_e32 v81, 0xbfb8aa3b, v79
	v_exp_f32_e32 v76, v76
	v_exp_f32_e32 v77, v77
	v_exp_f32_e32 v80, v80
	v_exp_f32_e32 v81, v81
	v_add_f32_e32 v68, 1.0, v68
	v_add_f32_e32 v69, 1.0, v69
	v_add_f32_e32 v72, 1.0, v72
	v_add_f32_e32 v73, 1.0, v73
	v_rcp_f32_e32 v68, v68
	v_rcp_f32_e32 v69, v69
	v_rcp_f32_e32 v72, v72
	v_rcp_f32_e32 v73, v73
	v_add_f32_e32 v76, 1.0, v76
	v_add_f32_e32 v77, 1.0, v77
	v_add_f32_e32 v80, 1.0, v80
	v_add_f32_e32 v81, 1.0, v81
	v_rcp_f32_e32 v76, v76
	v_rcp_f32_e32 v77, v77
	v_rcp_f32_e32 v80, v80
	v_rcp_f32_e32 v81, v81
	v_pk_mul_f32 v[66:67], v[68:69], v[66:67]
	v_pk_mul_f32 v[68:69], v[72:73], v[70:71]
	ds_write_b128 v170, v[66:69] offset:19584
	v_pk_mul_f32 v[66:67], v[76:77], v[74:75]
	v_pk_mul_f32 v[68:69], v[80:81], v[78:79]
	ds_write_b128 v170, v[66:69] offset:19600
	ds_write_b16 v171, v110 offset:26128
	ds_write_b16_d16_hi v171, v110 offset:26208
	ds_write_b16 v171, v111 offset:26288
	ds_write_b16_d16_hi v171, v111 offset:26368
	ds_write_b16 v171, v112 offset:26448
	ds_write_b16_d16_hi v171, v112 offset:26528
	ds_write_b16 v171, v113 offset:26608
	ds_write_b16_d16_hi v171, v113 offset:26688
	s_waitcnt vmcnt(37)
	v_lshlrev_b32_e32 v66, 16, v124
	v_and_b32_e32 v67, 0xffff0000, v124
	v_lshlrev_b32_e32 v68, 16, v125
	v_and_b32_e32 v69, 0xffff0000, v125
	v_lshlrev_b32_e32 v70, 16, v126
	v_and_b32_e32 v71, 0xffff0000, v126
	v_lshlrev_b32_e32 v72, 16, v127
	v_and_b32_e32 v73, 0xffff0000, v127
	ds_write_b128 v170, v[66:69] offset:4352
	s_waitcnt vmcnt(36)
	v_lshlrev_b32_e32 v66, 16, v128
	v_and_b32_e32 v67, 0xffff0000, v128
	ds_write_b128 v170, v[70:73] offset:4368
	v_lshlrev_b32_e32 v70, 16, v129
	v_and_b32_e32 v71, 0xffff0000, v129
	v_mul_f32_e32 v68, 0xbfb8aa3b, v66
	v_mul_f32_e32 v69, 0xbfb8aa3b, v67
	v_mul_f32_e32 v72, 0xbfb8aa3b, v70
	v_mul_f32_e32 v73, 0xbfb8aa3b, v71
	v_lshlrev_b32_e32 v74, 16, v130
	v_and_b32_e32 v75, 0xffff0000, v130
	v_lshlrev_b32_e32 v78, 16, v131
	v_and_b32_e32 v79, 0xffff0000, v131
	v_exp_f32_e32 v68, v68
	v_exp_f32_e32 v69, v69
	v_exp_f32_e32 v72, v72
	v_exp_f32_e32 v73, v73
	v_mul_f32_e32 v76, 0xbfb8aa3b, v74
	v_mul_f32_e32 v77, 0xbfb8aa3b, v75
	v_mul_f32_e32 v80, 0xbfb8aa3b, v78
	v_mul_f32_e32 v81, 0xbfb8aa3b, v79
	v_exp_f32_e32 v76, v76
	v_exp_f32_e32 v77, v77
	v_exp_f32_e32 v80, v80
	v_exp_f32_e32 v81, v81
	v_add_f32_e32 v68, 1.0, v68
	v_add_f32_e32 v69, 1.0, v69
	v_add_f32_e32 v72, 1.0, v72
	v_add_f32_e32 v73, 1.0, v73
	v_rcp_f32_e32 v68, v68
	v_rcp_f32_e32 v69, v69
	v_rcp_f32_e32 v72, v72
	v_rcp_f32_e32 v73, v73
	v_add_f32_e32 v76, 1.0, v76
	v_add_f32_e32 v77, 1.0, v77
	v_add_f32_e32 v80, 1.0, v80
	v_add_f32_e32 v81, 1.0, v81
	v_rcp_f32_e32 v76, v76
	v_rcp_f32_e32 v77, v77
	v_rcp_f32_e32 v80, v80
	v_rcp_f32_e32 v81, v81
	v_pk_mul_f32 v[66:67], v[68:69], v[66:67]
	v_pk_mul_f32 v[68:69], v[72:73], v[70:71]
	ds_write_b128 v170, v[66:69] offset:21760
	v_pk_mul_f32 v[66:67], v[76:77], v[74:75]
	v_pk_mul_f32 v[68:69], v[80:81], v[78:79]
	ds_write_b128 v170, v[66:69] offset:21776
	s_waitcnt vmcnt(33)
	ds_write_b16 v171, v140 offset:26144
	ds_write_b16_d16_hi v171, v140 offset:26224
	ds_write_b16 v171, v141 offset:26304
	ds_write_b16_d16_hi v171, v141 offset:26384
	ds_write_b16 v171, v142 offset:26464
	ds_write_b16_d16_hi v171, v142 offset:26544
	ds_write_b16 v171, v143 offset:26624
	ds_write_b16_d16_hi v171, v143 offset:26704
	v_lshlrev_b32_e32 v66, 16, v132
	v_and_b32_e32 v67, 0xffff0000, v132
	v_lshlrev_b32_e32 v68, 16, v133
	v_and_b32_e32 v69, 0xffff0000, v133
	v_lshlrev_b32_e32 v70, 16, v134
	v_and_b32_e32 v71, 0xffff0000, v134
	v_lshlrev_b32_e32 v72, 16, v135
	v_and_b32_e32 v73, 0xffff0000, v135
	ds_write_b128 v170, v[66:69] offset:6528
	s_waitcnt vmcnt(32)
	v_lshlrev_b32_e32 v66, 16, v144
	v_and_b32_e32 v67, 0xffff0000, v144
	ds_write_b128 v170, v[70:73] offset:6544
	v_lshlrev_b32_e32 v70, 16, v145
	v_and_b32_e32 v71, 0xffff0000, v145
	v_mul_f32_e32 v68, 0xbfb8aa3b, v66
	v_mul_f32_e32 v69, 0xbfb8aa3b, v67
	v_mul_f32_e32 v72, 0xbfb8aa3b, v70
	v_mul_f32_e32 v73, 0xbfb8aa3b, v71
	v_lshlrev_b32_e32 v74, 16, v146
	v_and_b32_e32 v75, 0xffff0000, v146
	v_lshlrev_b32_e32 v78, 16, v147
	v_and_b32_e32 v79, 0xffff0000, v147
	v_exp_f32_e32 v68, v68
	v_exp_f32_e32 v69, v69
	v_exp_f32_e32 v72, v72
	v_exp_f32_e32 v73, v73
	v_mul_f32_e32 v76, 0xbfb8aa3b, v74
	v_mul_f32_e32 v77, 0xbfb8aa3b, v75
	v_mul_f32_e32 v80, 0xbfb8aa3b, v78
	v_mul_f32_e32 v81, 0xbfb8aa3b, v79
	v_exp_f32_e32 v76, v76
	v_exp_f32_e32 v77, v77
	v_exp_f32_e32 v80, v80
	v_exp_f32_e32 v81, v81
	v_add_f32_e32 v68, 1.0, v68
	v_add_f32_e32 v69, 1.0, v69
	v_add_f32_e32 v72, 1.0, v72
	v_add_f32_e32 v73, 1.0, v73
	v_rcp_f32_e32 v68, v68
	v_rcp_f32_e32 v69, v69
	v_rcp_f32_e32 v72, v72
	v_rcp_f32_e32 v73, v73
	v_add_f32_e32 v76, 1.0, v76
	v_add_f32_e32 v77, 1.0, v77
	v_add_f32_e32 v80, 1.0, v80
	v_add_f32_e32 v81, 1.0, v81
	v_rcp_f32_e32 v76, v76
	v_rcp_f32_e32 v77, v77
	v_rcp_f32_e32 v80, v80
	v_rcp_f32_e32 v81, v81
	s_lshl_b32 s1, s0, 5
	v_pk_mul_f32 v[66:67], v[68:69], v[66:67]
	v_pk_mul_f32 v[68:69], v[72:73], v[70:71]
	s_add_i32 s1, s1, s3
	ds_write_b128 v170, v[66:69] offset:23936
	v_pk_mul_f32 v[66:67], v[76:77], v[74:75]
	v_pk_mul_f32 v[68:69], v[80:81], v[78:79]
	s_cmp_eq_u32 s0, 3
	ds_write_b128 v170, v[66:69] offset:23952
	ds_write_b16 v171, v136 offset:26160
	ds_write_b16_d16_hi v171, v136 offset:26240
	ds_write_b16 v171, v137 offset:26320
	ds_write_b16_d16_hi v171, v137 offset:26400
	ds_write_b16 v171, v138 offset:26480
	ds_write_b16_d16_hi v171, v138 offset:26560
	ds_write_b16 v171, v139 offset:26640
	ds_write_b16_d16_hi v171, v139 offset:26720
	s_cbranch_scc1 .LBB0_1000
	v_add_u32_e32 v66, s1, v182
	v_mad_i64_i32 v[66:67], s[22:23], v66, s96, v[168:169]
	v_add_co_u32_e32 v68, vcc, 0x9000, v66
	global_load_dwordx4 v[98:101], v[66:67], off offset:1728
	global_load_dwordx4 v[102:105], v[66:67], off offset:1216
	v_addc_co_u32_e32 v69, vcc, 0, v67, vcc
	global_load_dwordx4 v[106:109], v[68:69], off offset:1728
	global_load_dwordx4 v[110:113], v[68:69], off offset:2240
	global_load_dwordx4 v[116:119], v[66:67], off offset:2240
	global_load_dwordx4 v[120:123], v[68:69], off offset:1216
	v_add_co_u32_e32 v68, vcc, 0x12000, v66
	s_nop 1
	v_addc_co_u32_e32 v69, vcc, 0, v67, vcc
	v_add_co_u32_e32 v66, vcc, 0x1b000, v66
	global_load_dwordx4 v[124:127], v[68:69], off offset:1728
	global_load_dwordx4 v[128:131], v[68:69], off offset:1216
	v_addc_co_u32_e32 v67, vcc, 0, v67, vcc
	global_load_dwordx4 v[132:135], v[66:67], off offset:1728
	global_load_dwordx4 v[136:139], v[66:67], off offset:2240
	global_load_dwordx4 v[140:143], v[68:69], off offset:2240
	global_load_dwordx4 v[144:147], v[66:67], off offset:1216
